# P1 epilogue: row-sum partial store address computed once per unit, 12 of 16 store blocks reduced to one store
# baseline (speedup 1.0000x reference)
.LBB2_50:
	s_mul_i32 s0, s65, 0xc00
	v_cvt_f32_i32_e32 v149, v125
	v_cvt_f32_i32_e32 v148, v124
	v_cvt_f32_i32_e32 v151, v127
	v_cvt_f32_i32_e32 v150, v126
	s_add_i32 s0, s0, 0
	s_add_i32 s4, s0, 0x20000
	v_lshl_or_b32 v144, s64, 8, v202
	v_lshl_add_u32 v146, s23, 8, v201
	s_mov_b64 s[0:1], -1
	s_and_b64 vcc, exec, s[30:31]
	v_ashrrev_i32_e32 v145, 31, v144
	v_lshl_add_u32 v163, v202, 2, s4
	v_lshl_add_u32 v162, v201, 2, s4
	s_cbranch_vccz .LBB2_86
	ds_read2st64_b32 v[152:153], v162 offset1:4
	ds_read_b128 v[136:139], v163 offset:2048
	ds_read_b128 v[132:135], v163 offset:2064
	ds_read_b128 v[128:131], v163 offset:2080
	ds_read_b128 v[124:127], v163 offset:2096
	s_waitcnt lgkmcnt(4)
	v_mov_b32_e32 v154, v153
	v_mov_b32_e32 v153, v152
	v_mov_b32_e32 v155, v154
	s_waitcnt lgkmcnt(3)
	v_pk_mul_f32 v[140:141], v[138:139], v[150:151]
	v_pk_mul_f32 v[142:143], v[136:137], v[148:149]
	s_cmp_gt_i32 s23, 7
	v_pk_fma_f32 v[156:157], v[142:143], v[152:153], v[154:155] op_sel_hi:[1,0,0]
	v_pk_fma_f32 v[158:159], v[140:141], v[152:153], v[154:155] op_sel_hi:[1,0,0]
	s_cbranch_scc0 .LBB2_67
	v_cvt_f32_i32_e32 v141, v121
	v_cvt_f32_i32_e32 v143, v123
	v_cvt_f32_i32_e32 v142, v122
	v_cvt_f32_i32_e32 v140, v120
	v_cvt_f32_i32_e32 v169, v119
	v_cvt_f32_i32_e32 v168, v118
	s_waitcnt lgkmcnt(2)
	v_pk_mul_f32 v[142:143], v[134:135], v[142:143]
	v_pk_mul_f32 v[140:141], v[132:133], v[140:141]
	v_mov_b32_e32 v160, v154
	v_mov_b32_e32 v161, v154
	v_mov_b32_e32 v164, v152
	v_mov_b32_e32 v165, v152
	v_cvt_f32_i32_e32 v167, v117
	v_cvt_f32_i32_e32 v166, v116
	v_pk_fma_f32 v[170:171], v[142:143], v[164:165], v[160:161]
	v_pk_fma_f32 v[142:143], v[140:141], v[152:153], v[154:155]
	s_waitcnt lgkmcnt(1)
	v_pk_mul_f32 v[140:141], v[130:131], v[168:169]
	v_cvt_f32_i32_e32 v173, v113
	v_cvt_f32_i32_e32 v172, v112
	v_pk_fma_f32 v[168:169], v[140:141], v[164:165], v[160:161]
	v_pk_mul_f32 v[166:167], v[128:129], v[166:167]
	v_cvt_pk_fp8_f32 v140, v156, v157
	v_cvt_pk_fp8_f32 v141, v142, v143
	v_cvt_f32_i32_e32 v175, v115
	v_cvt_f32_i32_e32 v174, v114
	s_waitcnt lgkmcnt(0)
	v_pk_mul_f32 v[172:173], v[124:125], v[172:173]
	v_pk_fma_f32 v[166:167], v[166:167], v[152:153], v[154:155]
	v_pk_fma_f32 v[172:173], v[172:173], v[152:153], v[154:155]
	v_cvt_pk_fp8_f32 v140, v158, v159 op_sel:[0,0,1]
	v_cvt_pk_fp8_f32 v142, v166, v167
	v_cvt_pk_fp8_f32 v143, v172, v173
	v_cvt_pk_fp8_f32 v141, v170, v171 op_sel:[0,0,1]
	v_pk_mul_f32 v[174:175], v[126:127], v[174:175]
	v_cvt_pk_fp8_f32 v142, v168, v169 op_sel:[0,0,1]
	v_pk_fma_f32 v[160:161], v[174:175], v[164:165], v[160:161]
	s_mov_b32 s23, s22
	v_cvt_pk_fp8_f32 v143, v160, v161 op_sel:[0,0,1]
	v_mov_b64_e32 v[168:169], s[22:23]
	v_mov_b32_e32 v147, v195
	v_lshlrev_b64 v[160:161], 13, v[146:147]
	v_mfma_f32_16x16x32_fp8_fp8 v[164:167], v[140:141], v[168:169], 0
	v_lshl_add_u64 v[160:161], s[10:11], 0, v[160:161]
	v_lshl_add_u64 v[160:161], v[160:161], 0, v[144:145]
	global_store_dwordx4 v[160:161], v[140:143], off sc1
	s_nop 1
	v_mfma_f32_16x16x32_fp8_fp8 v[140:143], v[142:143], v[168:169], v[164:167]
	s_and_saveexec_b64 s[0:1], s[20:21]
	s_cbranch_execz .LBB2_54
	s_lshl_b32 s4, s64, 2
	s_or_b32 s4, s4, s46
	s_ashr_i32 s5, s4, 31
	s_lshl_b64 s[4:5], s[4:5], 14
	s_add_u32 s4, s2, s4
	s_addc_u32 s5, s3, s5
	v_lshl_add_u64 v[212:213], v[146:147], 2, s[4:5]
	v_lshlrev_b32_e32 v194, 2, v192
	v_lshl_add_u64 v[212:213], v[212:213], 0, v[194:195]
	global_store_dwordx4 v[212:213], v[140:143], off sc1
.LBB2_54:
	s_or_b64 exec, exec, s[0:1]
	v_add_u32_e32 v160, 64, v162
	ds_read2st64_b32 v[164:165], v160 offset1:4
	s_nop 2
	v_cvt_f32_i32_e32 v141, v109
	v_cvt_f32_i32_e32 v140, v108
	v_cvt_f32_i32_e32 v171, v107
	v_cvt_f32_i32_e32 v170, v106
	v_cvt_f32_i32_e32 v175, v103
	v_cvt_f32_i32_e32 v174, v102
	v_cvt_f32_i32_e32 v169, v105
	v_cvt_f32_i32_e32 v168, v104
	v_pk_mul_f32 v[140:141], v[136:137], v[140:141]
	s_waitcnt lgkmcnt(0)
	v_mov_b32_e32 v166, v165
	v_pk_fma_f32 v[172:173], v[140:141], v[164:165], v[166:167] op_sel_hi:[1,0,0]
	v_pk_mul_f32 v[140:141], v[134:135], v[170:171]
	v_cvt_f32_i32_e32 v143, v111
	v_cvt_f32_i32_e32 v142, v110
	v_pk_fma_f32 v[176:177], v[140:141], v[164:165], v[166:167] op_sel_hi:[1,0,0]
	v_pk_mul_f32 v[140:141], v[130:131], v[174:175]
	v_pk_mul_f32 v[168:169], v[132:133], v[168:169]
	v_cvt_f32_i32_e32 v171, v101
	v_cvt_f32_i32_e32 v170, v100
	v_pk_fma_f32 v[174:175], v[140:141], v[164:165], v[166:167] op_sel_hi:[1,0,0]
	v_cvt_f32_i32_e32 v179, v93
	v_cvt_f32_i32_e32 v178, v92
	v_pk_fma_f32 v[168:169], v[168:169], v[164:165], v[166:167] op_sel_hi:[1,0,0]
	v_cvt_pk_fp8_f32 v140, v172, v173
	v_pk_mul_f32 v[142:143], v[138:139], v[142:143]
	v_cvt_pk_fp8_f32 v141, v168, v169
	v_pk_fma_f32 v[142:143], v[142:143], v[164:165], v[166:167] op_sel_hi:[1,0,0]
	v_pk_mul_f32 v[170:171], v[128:129], v[170:171]
	v_cvt_f32_i32_e32 v181, v95
	v_cvt_f32_i32_e32 v180, v94
	v_pk_mul_f32 v[168:169], v[124:125], v[178:179]
	v_pk_fma_f32 v[170:171], v[170:171], v[164:165], v[166:167] op_sel_hi:[1,0,0]
	v_pk_fma_f32 v[168:169], v[168:169], v[164:165], v[166:167] op_sel_hi:[1,0,0]
	v_cvt_pk_fp8_f32 v140, v142, v143 op_sel:[0,0,1]
	v_cvt_pk_fp8_f32 v141, v176, v177 op_sel:[0,0,1]
	v_cvt_pk_fp8_f32 v142, v170, v171
	v_cvt_pk_fp8_f32 v143, v168, v169
	v_pk_mul_f32 v[168:169], v[126:127], v[180:181]
	v_mov_b64_e32 v[170:171], s[22:23]
	v_pk_fma_f32 v[164:165], v[168:169], v[164:165], v[166:167] op_sel_hi:[1,0,0]
	v_cvt_pk_fp8_f32 v142, v174, v175 op_sel:[0,0,1]
	v_cvt_pk_fp8_f32 v143, v164, v165 op_sel:[0,0,1]
	v_or_b32_e32 v194, 16, v146
	v_mfma_f32_16x16x32_fp8_fp8 v[164:167], v[140:141], v[170:171], 0
	v_lshlrev_b64 v[168:169], 13, v[194:195]
	v_lshl_add_u64 v[168:169], s[10:11], 0, v[168:169]
	v_lshl_add_u64 v[168:169], v[168:169], 0, v[144:145]
	global_store_dwordx4 v[168:169], v[140:143], off sc1
	s_nop 1
	v_mfma_f32_16x16x32_fp8_fp8 v[140:143], v[142:143], v[170:171], v[164:167]
	s_and_saveexec_b64 s[0:1], s[20:21]
	s_nop 6
	global_store_dwordx4 v[212:213], v[140:143], off offset:64 sc1
	s_or_b64 exec, exec, s[0:1]
	v_add_u32_e32 v161, 0x80, v162
	ds_read2st64_b32 v[164:165], v161 offset1:4
	s_nop 2
	v_cvt_f32_i32_e32 v141, v97
	v_cvt_f32_i32_e32 v140, v96
	v_cvt_f32_i32_e32 v171, v91
	v_cvt_f32_i32_e32 v170, v90
	v_cvt_f32_i32_e32 v175, v87
	v_cvt_f32_i32_e32 v174, v86
	v_cvt_f32_i32_e32 v169, v89
	v_cvt_f32_i32_e32 v168, v88
	v_pk_mul_f32 v[140:141], v[136:137], v[140:141]
	s_waitcnt lgkmcnt(0)
	v_mov_b32_e32 v166, v165
	v_pk_fma_f32 v[172:173], v[140:141], v[164:165], v[166:167] op_sel_hi:[1,0,0]
	v_pk_mul_f32 v[140:141], v[134:135], v[170:171]
	v_cvt_f32_i32_e32 v143, v99
	v_cvt_f32_i32_e32 v142, v98
	v_pk_fma_f32 v[176:177], v[140:141], v[164:165], v[166:167] op_sel_hi:[1,0,0]
	v_pk_mul_f32 v[140:141], v[130:131], v[174:175]
	v_pk_mul_f32 v[168:169], v[132:133], v[168:169]
	v_cvt_f32_i32_e32 v171, v85
	v_cvt_f32_i32_e32 v170, v84
	v_pk_fma_f32 v[178:179], v[140:141], v[164:165], v[166:167] op_sel_hi:[1,0,0]
	v_cvt_f32_i32_e32 v181, v77
	v_cvt_f32_i32_e32 v180, v76
	v_pk_fma_f32 v[168:169], v[168:169], v[164:165], v[166:167] op_sel_hi:[1,0,0]
	v_cvt_pk_fp8_f32 v140, v172, v173
	v_pk_mul_f32 v[142:143], v[138:139], v[142:143]
	v_cvt_pk_fp8_f32 v141, v168, v169
	v_pk_fma_f32 v[142:143], v[142:143], v[164:165], v[166:167] op_sel_hi:[1,0,0]
	v_pk_mul_f32 v[170:171], v[128:129], v[170:171]
	v_cvt_f32_i32_e32 v175, v79
	v_cvt_f32_i32_e32 v174, v78
	v_pk_mul_f32 v[168:169], v[124:125], v[180:181]
	v_pk_fma_f32 v[170:171], v[170:171], v[164:165], v[166:167] op_sel_hi:[1,0,0]
	v_pk_fma_f32 v[168:169], v[168:169], v[164:165], v[166:167] op_sel_hi:[1,0,0]
	v_cvt_pk_fp8_f32 v140, v142, v143 op_sel:[0,0,1]
	v_cvt_pk_fp8_f32 v141, v176, v177 op_sel:[0,0,1]
	v_cvt_pk_fp8_f32 v142, v170, v171
	v_cvt_pk_fp8_f32 v143, v168, v169
	v_pk_mul_f32 v[174:175], v[126:127], v[174:175]
	s_mov_b32 s23, s22
	v_pk_fma_f32 v[164:165], v[174:175], v[164:165], v[166:167] op_sel_hi:[1,0,0]
	v_cvt_pk_fp8_f32 v142, v178, v179 op_sel:[0,0,1]
	v_cvt_pk_fp8_f32 v143, v164, v165 op_sel:[0,0,1]
	v_mov_b64_e32 v[170:171], s[22:23]
	v_or_b32_e32 v194, 32, v146
	v_lshlrev_b64 v[168:169], 13, v[194:195]
	v_mfma_f32_16x16x32_fp8_fp8 v[164:167], v[140:141], v[170:171], 0
	v_lshl_add_u64 v[168:169], s[10:11], 0, v[168:169]
	v_lshl_add_u64 v[168:169], v[168:169], 0, v[144:145]
	global_store_dwordx4 v[168:169], v[140:143], off sc1
	s_nop 1
	v_mfma_f32_16x16x32_fp8_fp8 v[140:143], v[142:143], v[170:171], v[164:167]
	s_and_saveexec_b64 s[0:1], s[20:21]
	s_nop 6
	global_store_dwordx4 v[212:213], v[140:143], off offset:128 sc1
	s_or_b64 exec, exec, s[0:1]
	v_add_u32_e32 v164, 0xc0, v162
	ds_read2st64_b32 v[166:167], v164 offset1:4
	s_nop 2
	v_cvt_f32_i32_e32 v141, v81
	v_cvt_f32_i32_e32 v140, v80
	v_cvt_f32_i32_e32 v173, v75
	v_cvt_f32_i32_e32 v172, v74
	v_cvt_f32_i32_e32 v177, v71
	v_cvt_f32_i32_e32 v176, v70
	v_cvt_f32_i32_e32 v171, v73
	v_cvt_f32_i32_e32 v170, v72
	v_pk_mul_f32 v[140:141], v[136:137], v[140:141]
	s_waitcnt lgkmcnt(0)
	v_mov_b32_e32 v168, v167
	v_pk_fma_f32 v[174:175], v[140:141], v[166:167], v[168:169] op_sel_hi:[1,0,0]
	v_pk_mul_f32 v[140:141], v[134:135], v[172:173]
	v_cvt_f32_i32_e32 v143, v83
	v_cvt_f32_i32_e32 v142, v82
	v_pk_fma_f32 v[178:179], v[140:141], v[166:167], v[168:169] op_sel_hi:[1,0,0]
	v_pk_mul_f32 v[140:141], v[130:131], v[176:177]
	v_pk_mul_f32 v[170:171], v[132:133], v[170:171]
	v_cvt_f32_i32_e32 v173, v69
	v_cvt_f32_i32_e32 v172, v68
	v_pk_fma_f32 v[176:177], v[140:141], v[166:167], v[168:169] op_sel_hi:[1,0,0]
	v_cvt_f32_i32_e32 v181, v65
	v_cvt_f32_i32_e32 v180, v64
	v_pk_fma_f32 v[170:171], v[170:171], v[166:167], v[168:169] op_sel_hi:[1,0,0]
	v_cvt_pk_fp8_f32 v140, v174, v175
	v_pk_mul_f32 v[142:143], v[138:139], v[142:143]
	v_cvt_pk_fp8_f32 v141, v170, v171
	v_pk_fma_f32 v[142:143], v[142:143], v[166:167], v[168:169] op_sel_hi:[1,0,0]
	v_pk_mul_f32 v[172:173], v[128:129], v[172:173]
	v_cvt_f32_i32_e32 v183, v67
	v_cvt_f32_i32_e32 v182, v66
	v_pk_mul_f32 v[170:171], v[124:125], v[180:181]
	v_pk_fma_f32 v[172:173], v[172:173], v[166:167], v[168:169] op_sel_hi:[1,0,0]
	v_pk_fma_f32 v[170:171], v[170:171], v[166:167], v[168:169] op_sel_hi:[1,0,0]
	v_cvt_pk_fp8_f32 v140, v142, v143 op_sel:[0,0,1]
	v_cvt_pk_fp8_f32 v141, v178, v179 op_sel:[0,0,1]
	v_cvt_pk_fp8_f32 v142, v172, v173
	v_cvt_pk_fp8_f32 v143, v170, v171
	v_pk_mul_f32 v[170:171], v[126:127], v[182:183]
	v_mov_b64_e32 v[172:173], s[22:23]
	v_pk_fma_f32 v[166:167], v[170:171], v[166:167], v[168:169] op_sel_hi:[1,0,0]
	v_cvt_pk_fp8_f32 v142, v176, v177 op_sel:[0,0,1]
	v_cvt_pk_fp8_f32 v143, v166, v167 op_sel:[0,0,1]
	v_or_b32_e32 v194, 48, v146
	v_mfma_f32_16x16x32_fp8_fp8 v[166:169], v[140:141], v[172:173], 0
	v_lshlrev_b64 v[170:171], 13, v[194:195]
	v_lshl_add_u64 v[170:171], s[10:11], 0, v[170:171]
	v_lshl_add_u64 v[170:171], v[170:171], 0, v[144:145]
	global_store_dwordx4 v[170:171], v[140:143], off sc1
	s_nop 1
	v_mfma_f32_16x16x32_fp8_fp8 v[140:143], v[142:143], v[172:173], v[166:169]
	s_and_saveexec_b64 s[0:1], s[20:21]
	s_nop 6
	global_store_dwordx4 v[212:213], v[140:143], off offset:192 sc1
	s_or_b64 exec, exec, s[0:1]
	ds_read2st64_b32 v[166:167], v162 offset0:2 offset1:6
	s_nop 3
	v_cvt_f32_i32_e32 v141, v61
	v_cvt_f32_i32_e32 v140, v60
	v_cvt_f32_i32_e32 v173, v59
	v_cvt_f32_i32_e32 v172, v58
	v_cvt_f32_i32_e32 v177, v51
	v_cvt_f32_i32_e32 v176, v50
	v_cvt_f32_i32_e32 v171, v57
	v_cvt_f32_i32_e32 v170, v56
	v_pk_mul_f32 v[140:141], v[136:137], v[140:141]
	s_waitcnt lgkmcnt(0)
	v_mov_b32_e32 v168, v167
	v_pk_fma_f32 v[174:175], v[140:141], v[166:167], v[168:169] op_sel_hi:[1,0,0]
	v_pk_mul_f32 v[140:141], v[134:135], v[172:173]
	v_cvt_f32_i32_e32 v143, v63
	v_cvt_f32_i32_e32 v142, v62
	v_pk_fma_f32 v[178:179], v[140:141], v[166:167], v[168:169] op_sel_hi:[1,0,0]
	v_pk_mul_f32 v[140:141], v[130:131], v[176:177]
	v_pk_mul_f32 v[170:171], v[132:133], v[170:171]
	v_cvt_f32_i32_e32 v173, v49
	v_cvt_f32_i32_e32 v172, v48
	v_pk_fma_f32 v[176:177], v[140:141], v[166:167], v[168:169] op_sel_hi:[1,0,0]
	v_cvt_f32_i32_e32 v181, v41
	v_cvt_f32_i32_e32 v180, v40
	v_pk_fma_f32 v[170:171], v[170:171], v[166:167], v[168:169] op_sel_hi:[1,0,0]
	v_cvt_pk_fp8_f32 v140, v174, v175
	v_pk_mul_f32 v[142:143], v[138:139], v[142:143]
	v_cvt_pk_fp8_f32 v141, v170, v171
	v_pk_fma_f32 v[142:143], v[142:143], v[166:167], v[168:169] op_sel_hi:[1,0,0]
	v_pk_mul_f32 v[172:173], v[128:129], v[172:173]
	v_cvt_f32_i32_e32 v183, v43
	v_cvt_f32_i32_e32 v182, v42
	v_pk_mul_f32 v[170:171], v[124:125], v[180:181]
	v_pk_fma_f32 v[172:173], v[172:173], v[166:167], v[168:169] op_sel_hi:[1,0,0]
	v_pk_fma_f32 v[170:171], v[170:171], v[166:167], v[168:169] op_sel_hi:[1,0,0]
	v_cvt_pk_fp8_f32 v140, v142, v143 op_sel:[0,0,1]
	v_cvt_pk_fp8_f32 v141, v178, v179 op_sel:[0,0,1]
	v_cvt_pk_fp8_f32 v142, v172, v173
	v_cvt_pk_fp8_f32 v143, v170, v171
	v_pk_mul_f32 v[170:171], v[126:127], v[182:183]
	s_mov_b32 s23, s22
	v_pk_fma_f32 v[166:167], v[170:171], v[166:167], v[168:169] op_sel_hi:[1,0,0]
	v_cvt_pk_fp8_f32 v142, v176, v177 op_sel:[0,0,1]
	v_cvt_pk_fp8_f32 v143, v166, v167 op_sel:[0,0,1]
	v_mov_b64_e32 v[172:173], s[22:23]
	v_add_u32_e32 v194, 0x80, v146
	v_lshlrev_b64 v[170:171], 13, v[194:195]
	v_mfma_f32_16x16x32_fp8_fp8 v[166:169], v[140:141], v[172:173], 0
	v_lshl_add_u64 v[170:171], s[10:11], 0, v[170:171]
	v_lshl_add_u64 v[170:171], v[170:171], 0, v[144:145]
	global_store_dwordx4 v[170:171], v[140:143], off sc1
	s_nop 1
	v_mfma_f32_16x16x32_fp8_fp8 v[140:143], v[142:143], v[172:173], v[166:169]
	s_and_saveexec_b64 s[0:1], s[20:21]
	s_nop 6
	global_store_dwordx4 v[212:213], v[140:143], off offset:512 sc1
	s_or_b64 exec, exec, s[0:1]
	ds_read2st64_b32 v[166:167], v160 offset0:2 offset1:6
	s_nop 3
	v_cvt_f32_i32_e32 v141, v53
	v_cvt_f32_i32_e32 v140, v52
	v_cvt_f32_i32_e32 v171, v47
	v_cvt_f32_i32_e32 v170, v46
	v_cvt_f32_i32_e32 v175, v35
	v_cvt_f32_i32_e32 v174, v34
	v_cvt_f32_i32_e32 v169, v45
	v_cvt_f32_i32_e32 v168, v44
	v_pk_mul_f32 v[140:141], v[136:137], v[140:141]
	s_waitcnt lgkmcnt(0)
	v_mov_b32_e32 v160, v167
	v_pk_fma_f32 v[172:173], v[140:141], v[166:167], v[160:161] op_sel_hi:[1,0,0]
	v_pk_mul_f32 v[140:141], v[134:135], v[170:171]
	v_cvt_f32_i32_e32 v143, v55
	v_cvt_f32_i32_e32 v142, v54
	v_pk_fma_f32 v[176:177], v[140:141], v[166:167], v[160:161] op_sel_hi:[1,0,0]
	v_pk_mul_f32 v[140:141], v[130:131], v[174:175]
	v_pk_mul_f32 v[168:169], v[132:133], v[168:169]
	v_cvt_f32_i32_e32 v171, v33
	v_cvt_f32_i32_e32 v170, v32
	v_pk_fma_f32 v[174:175], v[140:141], v[166:167], v[160:161] op_sel_hi:[1,0,0]
	v_cvt_f32_i32_e32 v179, v25
	v_cvt_f32_i32_e32 v178, v24
	v_pk_fma_f32 v[168:169], v[168:169], v[166:167], v[160:161] op_sel_hi:[1,0,0]
	v_cvt_pk_fp8_f32 v140, v172, v173
	v_pk_mul_f32 v[142:143], v[138:139], v[142:143]
	v_cvt_pk_fp8_f32 v141, v168, v169
	v_pk_fma_f32 v[142:143], v[142:143], v[166:167], v[160:161] op_sel_hi:[1,0,0]
	v_pk_mul_f32 v[170:171], v[128:129], v[170:171]
	v_cvt_f32_i32_e32 v181, v27
	v_cvt_f32_i32_e32 v180, v26
	v_pk_mul_f32 v[168:169], v[124:125], v[178:179]
	v_pk_fma_f32 v[170:171], v[170:171], v[166:167], v[160:161] op_sel_hi:[1,0,0]
	v_pk_fma_f32 v[168:169], v[168:169], v[166:167], v[160:161] op_sel_hi:[1,0,0]
	v_cvt_pk_fp8_f32 v140, v142, v143 op_sel:[0,0,1]
	v_cvt_pk_fp8_f32 v141, v176, v177 op_sel:[0,0,1]
	v_cvt_pk_fp8_f32 v142, v170, v171
	v_cvt_pk_fp8_f32 v143, v168, v169
	v_pk_mul_f32 v[168:169], v[126:127], v[180:181]
	v_mov_b64_e32 v[172:173], s[22:23]
	v_pk_fma_f32 v[166:167], v[168:169], v[166:167], v[160:161] op_sel_hi:[1,0,0]
	v_cvt_pk_fp8_f32 v142, v174, v175 op_sel:[0,0,1]
	v_cvt_pk_fp8_f32 v143, v166, v167 op_sel:[0,0,1]
	v_add_u32_e32 v194, 0x90, v146
	v_mfma_f32_16x16x32_fp8_fp8 v[166:169], v[140:141], v[172:173], 0
	v_lshlrev_b64 v[170:171], 13, v[194:195]
	v_lshl_add_u64 v[170:171], s[10:11], 0, v[170:171]
	v_lshl_add_u64 v[170:171], v[170:171], 0, v[144:145]
	global_store_dwordx4 v[170:171], v[140:143], off sc1
	s_nop 1
	v_mfma_f32_16x16x32_fp8_fp8 v[140:143], v[142:143], v[172:173], v[166:169]
	s_and_saveexec_b64 s[0:1], s[20:21]
	s_nop 6
	global_store_dwordx4 v[212:213], v[140:143], off offset:576 sc1
	s_or_b64 exec, exec, s[0:1]
	ds_read2st64_b32 v[160:161], v161 offset0:2 offset1:6
	s_nop 3
	v_cvt_f32_i32_e32 v141, v37
	v_cvt_f32_i32_e32 v140, v36
	v_cvt_f32_i32_e32 v171, v31
	v_cvt_f32_i32_e32 v170, v30
	v_cvt_f32_i32_e32 v175, v19
	v_cvt_f32_i32_e32 v174, v18
	v_cvt_f32_i32_e32 v169, v29
	v_cvt_f32_i32_e32 v168, v28
	v_pk_mul_f32 v[140:141], v[136:137], v[140:141]
	s_waitcnt lgkmcnt(0)
	v_mov_b32_e32 v166, v161
	v_pk_fma_f32 v[172:173], v[140:141], v[160:161], v[166:167] op_sel_hi:[1,0,0]
	v_pk_mul_f32 v[140:141], v[134:135], v[170:171]
	v_cvt_f32_i32_e32 v143, v39
	v_cvt_f32_i32_e32 v142, v38
	v_pk_fma_f32 v[176:177], v[140:141], v[160:161], v[166:167] op_sel_hi:[1,0,0]
	v_pk_mul_f32 v[140:141], v[130:131], v[174:175]
	v_pk_mul_f32 v[168:169], v[132:133], v[168:169]
	v_cvt_f32_i32_e32 v171, v17
	v_cvt_f32_i32_e32 v170, v16
	v_pk_fma_f32 v[178:179], v[140:141], v[160:161], v[166:167] op_sel_hi:[1,0,0]
	v_cvt_f32_i32_e32 v181, v9
	v_cvt_f32_i32_e32 v180, v8
	v_pk_fma_f32 v[168:169], v[168:169], v[160:161], v[166:167] op_sel_hi:[1,0,0]
	v_cvt_pk_fp8_f32 v140, v172, v173
	v_pk_mul_f32 v[142:143], v[138:139], v[142:143]
	v_cvt_pk_fp8_f32 v141, v168, v169
	v_pk_fma_f32 v[142:143], v[142:143], v[160:161], v[166:167] op_sel_hi:[1,0,0]
	v_pk_mul_f32 v[170:171], v[128:129], v[170:171]
	v_cvt_f32_i32_e32 v175, v11
	v_cvt_f32_i32_e32 v174, v10
	v_pk_mul_f32 v[168:169], v[124:125], v[180:181]
	v_pk_fma_f32 v[170:171], v[170:171], v[160:161], v[166:167] op_sel_hi:[1,0,0]
	v_pk_fma_f32 v[168:169], v[168:169], v[160:161], v[166:167] op_sel_hi:[1,0,0]
	v_cvt_pk_fp8_f32 v140, v142, v143 op_sel:[0,0,1]
	v_cvt_pk_fp8_f32 v141, v176, v177 op_sel:[0,0,1]
	v_cvt_pk_fp8_f32 v142, v170, v171
	v_cvt_pk_fp8_f32 v143, v168, v169
	v_pk_mul_f32 v[174:175], v[126:127], v[174:175]
	s_mov_b32 s23, s22
	v_pk_fma_f32 v[160:161], v[174:175], v[160:161], v[166:167] op_sel_hi:[1,0,0]
	v_cvt_pk_fp8_f32 v142, v178, v179 op_sel:[0,0,1]
	v_cvt_pk_fp8_f32 v143, v160, v161 op_sel:[0,0,1]
	v_mov_b64_e32 v[170:171], s[22:23]
	v_add_u32_e32 v194, 0xa0, v146
	v_lshlrev_b64 v[160:161], 13, v[194:195]
	v_mfma_f32_16x16x32_fp8_fp8 v[166:169], v[140:141], v[170:171], 0
	v_lshl_add_u64 v[160:161], s[10:11], 0, v[160:161]
	v_lshl_add_u64 v[160:161], v[160:161], 0, v[144:145]
	global_store_dwordx4 v[160:161], v[140:143], off sc1
	s_nop 1
	v_mfma_f32_16x16x32_fp8_fp8 v[140:143], v[142:143], v[170:171], v[166:169]
	s_and_saveexec_b64 s[0:1], s[20:21]
	s_nop 6
	global_store_dwordx4 v[212:213], v[140:143], off offset:640 sc1
	s_or_b64 exec, exec, s[0:1]
	ds_read2st64_b32 v[160:161], v164 offset0:2 offset1:6
	s_nop 3
	v_cvt_f32_i32_e32 v141, v21
	v_cvt_f32_i32_e32 v140, v20
	v_cvt_f32_i32_e32 v169, v15
	v_cvt_f32_i32_e32 v168, v14
	v_cvt_f32_i32_e32 v173, v7
	v_cvt_f32_i32_e32 v172, v6
	v_cvt_f32_i32_e32 v167, v13
	v_cvt_f32_i32_e32 v166, v12
	v_pk_mul_f32 v[140:141], v[136:137], v[140:141]
	s_waitcnt lgkmcnt(0)
	v_mov_b32_e32 v164, v161
	v_pk_fma_f32 v[170:171], v[140:141], v[160:161], v[164:165] op_sel_hi:[1,0,0]
	v_pk_mul_f32 v[140:141], v[134:135], v[168:169]
	v_cvt_f32_i32_e32 v143, v23
	v_cvt_f32_i32_e32 v142, v22
	v_pk_fma_f32 v[174:175], v[140:141], v[160:161], v[164:165] op_sel_hi:[1,0,0]
	v_pk_mul_f32 v[140:141], v[130:131], v[172:173]
	v_pk_mul_f32 v[166:167], v[132:133], v[166:167]
	v_cvt_f32_i32_e32 v169, v5
	v_cvt_f32_i32_e32 v168, v4
	v_pk_fma_f32 v[172:173], v[140:141], v[160:161], v[164:165] op_sel_hi:[1,0,0]
	v_cvt_f32_i32_e32 v177, v1
	v_cvt_f32_i32_e32 v176, v0
	v_pk_fma_f32 v[166:167], v[166:167], v[160:161], v[164:165] op_sel_hi:[1,0,0]
	v_cvt_pk_fp8_f32 v140, v170, v171
	v_pk_mul_f32 v[142:143], v[138:139], v[142:143]
	v_cvt_pk_fp8_f32 v141, v166, v167
	v_pk_fma_f32 v[142:143], v[142:143], v[160:161], v[164:165] op_sel_hi:[1,0,0]
	v_pk_mul_f32 v[168:169], v[128:129], v[168:169]
	v_cvt_f32_i32_e32 v179, v3
	v_cvt_f32_i32_e32 v178, v2
	v_pk_mul_f32 v[166:167], v[124:125], v[176:177]
	v_pk_fma_f32 v[168:169], v[168:169], v[160:161], v[164:165] op_sel_hi:[1,0,0]
	v_pk_fma_f32 v[166:167], v[166:167], v[160:161], v[164:165] op_sel_hi:[1,0,0]
	v_cvt_pk_fp8_f32 v140, v142, v143 op_sel:[0,0,1]
	v_cvt_pk_fp8_f32 v141, v174, v175 op_sel:[0,0,1]
	v_cvt_pk_fp8_f32 v142, v168, v169
	v_cvt_pk_fp8_f32 v143, v166, v167
	v_pk_mul_f32 v[166:167], v[126:127], v[178:179]
	v_mov_b64_e32 v[168:169], s[22:23]
	v_pk_fma_f32 v[160:161], v[166:167], v[160:161], v[164:165] op_sel_hi:[1,0,0]
	v_cvt_pk_fp8_f32 v142, v172, v173 op_sel:[0,0,1]
	v_cvt_pk_fp8_f32 v143, v160, v161 op_sel:[0,0,1]
	v_add_u32_e32 v194, 0xb0, v146
	v_mfma_f32_16x16x32_fp8_fp8 v[164:167], v[140:141], v[168:169], 0
	v_lshlrev_b64 v[160:161], 13, v[194:195]
	v_lshl_add_u64 v[160:161], s[10:11], 0, v[160:161]
	v_lshl_add_u64 v[160:161], v[160:161], 0, v[144:145]
	global_store_dwordx4 v[160:161], v[140:143], off sc1
	s_mov_b64 s[0:1], s[20:21]
	s_nop 0
	v_mfma_f32_16x16x32_fp8_fp8 v[140:143], v[142:143], v[168:169], v[164:167]
	v_mov_b64_e32 v[160:161], v[194:195]
	s_branch .LBB2_83
.LBB2_67:
	s_mov_b64 s[0:1], 0
	s_cbranch_execz .LBB2_83
	v_cvt_f32_i32_e32 v141, v121
	v_cvt_f32_i32_e32 v143, v123
	v_cvt_f32_i32_e32 v142, v122
	v_cvt_f32_i32_e32 v140, v120
	v_cvt_f32_i32_e32 v169, v119
	v_cvt_f32_i32_e32 v168, v118
	s_waitcnt lgkmcnt(2)
	v_pk_mul_f32 v[142:143], v[134:135], v[142:143]
	v_pk_mul_f32 v[140:141], v[132:133], v[140:141]
	v_mov_b32_e32 v160, v154
	v_mov_b32_e32 v161, v154
	v_mov_b32_e32 v164, v152
	v_mov_b32_e32 v165, v152
	v_pk_fma_f32 v[142:143], v[142:143], v[164:165], v[160:161]
	v_pk_fma_f32 v[140:141], v[140:141], v[152:153], v[154:155]
	v_cvt_f32_i32_e32 v167, v117
	v_cvt_f32_i32_e32 v166, v116
	v_pk_mul_f32 v[170:171], v[142:143], v[142:143]
	v_pk_mul_f32 v[142:143], v[140:141], v[140:141]
	s_waitcnt lgkmcnt(1)
	v_pk_mul_f32 v[140:141], v[130:131], v[168:169]
	v_cvt_f32_i32_e32 v169, v113
	v_cvt_f32_i32_e32 v168, v112
	v_pk_fma_f32 v[140:141], v[140:141], v[164:165], v[160:161]
	v_pk_mul_f32 v[156:157], v[156:157], v[156:157]
	v_pk_mul_f32 v[174:175], v[140:141], v[140:141]
	v_pk_mul_f32 v[166:167], v[128:129], v[166:167]
	v_cvt_pk_fp8_f32 v140, v156, v157
	v_cvt_pk_fp8_f32 v141, v142, v143
	v_cvt_f32_i32_e32 v173, v115
	v_cvt_f32_i32_e32 v172, v114
	s_waitcnt lgkmcnt(0)
	v_pk_mul_f32 v[168:169], v[124:125], v[168:169]
	v_pk_fma_f32 v[166:167], v[166:167], v[152:153], v[154:155]
	v_pk_fma_f32 v[152:153], v[168:169], v[152:153], v[154:155]
	v_pk_mul_f32 v[158:159], v[158:159], v[158:159]
	v_pk_mul_f32 v[166:167], v[166:167], v[166:167]
	v_pk_mul_f32 v[152:153], v[152:153], v[152:153]
	v_cvt_pk_fp8_f32 v140, v158, v159 op_sel:[0,0,1]
	v_cvt_pk_fp8_f32 v142, v166, v167
	v_cvt_pk_fp8_f32 v143, v152, v153
	v_cvt_pk_fp8_f32 v141, v170, v171 op_sel:[0,0,1]
	v_pk_mul_f32 v[172:173], v[126:127], v[172:173]
	v_cvt_pk_fp8_f32 v142, v174, v175 op_sel:[0,0,1]
	v_pk_fma_f32 v[156:157], v[172:173], v[164:165], v[160:161]
	s_mov_b32 s23, s22
	v_pk_mul_f32 v[152:153], v[156:157], v[156:157]
	v_mov_b64_e32 v[158:159], s[22:23]
	v_cvt_pk_fp8_f32 v143, v152, v153 op_sel:[0,0,1]
	v_ashrrev_i32_e32 v147, 31, v146
	v_mfma_f32_16x16x32_fp8_fp8 v[152:155], v[140:141], v[158:159], 0
	v_lshlrev_b64 v[156:157], 13, v[146:147]
	v_lshl_add_u64 v[156:157], s[10:11], 0, v[156:157]
	v_lshl_add_u64 v[156:157], v[156:157], 0, v[144:145]
	global_store_dwordx4 v[156:157], v[140:143], off sc1
	s_nop 1
	v_mfma_f32_16x16x32_fp8_fp8 v[140:143], v[142:143], v[158:159], v[152:155]
	s_and_saveexec_b64 s[0:1], s[20:21]
	s_cbranch_execz .LBB2_70
	s_lshl_b32 s4, s64, 2
	s_or_b32 s4, s4, s46
	s_ashr_i32 s5, s4, 31
	s_lshl_b64 s[4:5], s[4:5], 14
	s_add_u32 s4, s2, s4
	s_addc_u32 s5, s3, s5
	v_lshl_add_u64 v[212:213], v[146:147], 2, s[4:5]
	v_lshlrev_b32_e32 v194, 2, v192
	v_lshl_add_u64 v[212:213], v[212:213], 0, v[194:195]
	global_store_dwordx4 v[212:213], v[140:143], off sc1
.LBB2_70:
	s_or_b64 exec, exec, s[0:1]
	v_add_u32_e32 v154, 64, v162
	s_nop 3
	ds_read2st64_b32 v[142:143], v154 offset1:4
	v_cvt_f32_i32_e32 v141, v109
	v_cvt_f32_i32_e32 v140, v108
	v_cvt_f32_i32_e32 v161, v107
	v_cvt_f32_i32_e32 v160, v106
	s_waitcnt lgkmcnt(0)
	v_mov_b32_e32 v156, v143
	v_pk_mul_f32 v[140:141], v[136:137], v[140:141]
	v_cvt_f32_i32_e32 v167, v103
	v_cvt_f32_i32_e32 v166, v102
	v_pk_fma_f32 v[140:141], v[140:141], v[142:143], v[156:157] op_sel_hi:[1,0,0]
	v_cvt_f32_i32_e32 v159, v105
	v_pk_mul_f32 v[164:165], v[140:141], v[140:141]
	v_pk_mul_f32 v[140:141], v[134:135], v[160:161]
	v_cvt_f32_i32_e32 v158, v104
	v_pk_fma_f32 v[140:141], v[140:141], v[142:143], v[156:157] op_sel_hi:[1,0,0]
	v_cvt_f32_i32_e32 v153, v111
	v_pk_mul_f32 v[168:169], v[140:141], v[140:141]
	v_pk_mul_f32 v[140:141], v[130:131], v[166:167]
	v_cvt_f32_i32_e32 v167, v93
	v_cvt_f32_i32_e32 v166, v92
	v_cvt_f32_i32_e32 v152, v110
	v_pk_mul_f32 v[158:159], v[132:133], v[158:159]
	v_cvt_f32_i32_e32 v161, v101
	v_cvt_f32_i32_e32 v160, v100
	v_pk_fma_f32 v[140:141], v[140:141], v[142:143], v[156:157] op_sel_hi:[1,0,0]
	v_pk_fma_f32 v[158:159], v[158:159], v[142:143], v[156:157] op_sel_hi:[1,0,0]
	v_cvt_f32_i32_e32 v171, v95
	v_cvt_f32_i32_e32 v170, v94
	v_pk_mul_f32 v[172:173], v[140:141], v[140:141]
	v_pk_mul_f32 v[140:141], v[124:125], v[166:167]
	v_pk_mul_f32 v[158:159], v[158:159], v[158:159]
	v_pk_fma_f32 v[166:167], v[140:141], v[142:143], v[156:157] op_sel_hi:[1,0,0]
	v_pk_mul_f32 v[152:153], v[138:139], v[152:153]
	v_cvt_pk_fp8_f32 v140, v164, v165
	v_cvt_pk_fp8_f32 v141, v158, v159
	v_pk_mul_f32 v[160:161], v[128:129], v[160:161]
	v_pk_fma_f32 v[152:153], v[152:153], v[142:143], v[156:157] op_sel_hi:[1,0,0]
	v_pk_fma_f32 v[160:161], v[160:161], v[142:143], v[156:157] op_sel_hi:[1,0,0]
	v_pk_mul_f32 v[170:171], v[126:127], v[170:171]
	v_pk_mul_f32 v[152:153], v[152:153], v[152:153]
	v_pk_mul_f32 v[160:161], v[160:161], v[160:161]
	v_pk_fma_f32 v[156:157], v[170:171], v[142:143], v[156:157] op_sel_hi:[1,0,0]
	v_pk_mul_f32 v[158:159], v[166:167], v[166:167]
	v_cvt_pk_fp8_f32 v140, v152, v153 op_sel:[0,0,1]
	v_cvt_pk_fp8_f32 v141, v168, v169 op_sel:[0,0,1]
	v_cvt_pk_fp8_f32 v142, v160, v161
	v_cvt_pk_fp8_f32 v143, v158, v159
	v_pk_mul_f32 v[152:153], v[156:157], v[156:157]
	v_or_b32_e32 v156, 16, v146
	v_cvt_pk_fp8_f32 v142, v172, v173 op_sel:[0,0,1]
	v_cvt_pk_fp8_f32 v143, v152, v153 op_sel:[0,0,1]
	v_ashrrev_i32_e32 v157, 31, v156
	v_mov_b64_e32 v[160:161], s[22:23]
	v_lshlrev_b64 v[152:153], 13, v[156:157]
	v_lshl_add_u64 v[152:153], s[10:11], 0, v[152:153]
	v_mfma_f32_16x16x32_fp8_fp8 v[156:159], v[140:141], v[160:161], 0
	v_lshl_add_u64 v[152:153], v[152:153], 0, v[144:145]
	global_store_dwordx4 v[152:153], v[140:143], off sc1
	s_nop 1
	v_mfma_f32_16x16x32_fp8_fp8 v[140:143], v[142:143], v[160:161], v[156:159]
	s_and_saveexec_b64 s[0:1], s[20:21]
	s_nop 6
	global_store_dwordx4 v[212:213], v[140:143], off offset:64 sc1
	s_or_b64 exec, exec, s[0:1]
	v_add_u32_e32 v155, 0x80, v162
	s_nop 3
	ds_read2st64_b32 v[142:143], v155 offset1:4
	v_cvt_f32_i32_e32 v141, v97
	v_cvt_f32_i32_e32 v140, v96
	v_cvt_f32_i32_e32 v161, v91
	v_cvt_f32_i32_e32 v160, v90
	s_waitcnt lgkmcnt(0)
	v_mov_b32_e32 v156, v143
	v_pk_mul_f32 v[140:141], v[136:137], v[140:141]
	v_cvt_f32_i32_e32 v167, v87
	v_cvt_f32_i32_e32 v166, v86
	v_pk_fma_f32 v[140:141], v[140:141], v[142:143], v[156:157] op_sel_hi:[1,0,0]
	v_cvt_f32_i32_e32 v159, v89
	v_pk_mul_f32 v[164:165], v[140:141], v[140:141]
	v_pk_mul_f32 v[140:141], v[134:135], v[160:161]
	v_cvt_f32_i32_e32 v158, v88
	v_pk_fma_f32 v[140:141], v[140:141], v[142:143], v[156:157] op_sel_hi:[1,0,0]
	v_cvt_f32_i32_e32 v153, v99
	v_pk_mul_f32 v[168:169], v[140:141], v[140:141]
	v_pk_mul_f32 v[140:141], v[130:131], v[166:167]
	v_cvt_f32_i32_e32 v167, v77
	v_cvt_f32_i32_e32 v166, v76
	v_cvt_f32_i32_e32 v152, v98
	v_pk_mul_f32 v[158:159], v[132:133], v[158:159]
	v_cvt_f32_i32_e32 v161, v85
	v_cvt_f32_i32_e32 v160, v84
	v_pk_fma_f32 v[140:141], v[140:141], v[142:143], v[156:157] op_sel_hi:[1,0,0]
	v_cvt_f32_i32_e32 v171, v79
	v_cvt_f32_i32_e32 v170, v78
	v_pk_fma_f32 v[158:159], v[158:159], v[142:143], v[156:157] op_sel_hi:[1,0,0]
	v_pk_mul_f32 v[172:173], v[140:141], v[140:141]
	v_pk_mul_f32 v[140:141], v[124:125], v[166:167]
	v_pk_mul_f32 v[158:159], v[158:159], v[158:159]
	v_pk_fma_f32 v[166:167], v[140:141], v[142:143], v[156:157] op_sel_hi:[1,0,0]
	v_pk_mul_f32 v[152:153], v[138:139], v[152:153]
	v_cvt_pk_fp8_f32 v140, v164, v165
	v_cvt_pk_fp8_f32 v141, v158, v159
	v_pk_mul_f32 v[160:161], v[128:129], v[160:161]
	v_pk_mul_f32 v[170:171], v[126:127], v[170:171]
	v_pk_fma_f32 v[152:153], v[152:153], v[142:143], v[156:157] op_sel_hi:[1,0,0]
	v_pk_fma_f32 v[160:161], v[160:161], v[142:143], v[156:157] op_sel_hi:[1,0,0]
	v_pk_fma_f32 v[142:143], v[170:171], v[142:143], v[156:157] op_sel_hi:[1,0,0]
	v_pk_mul_f32 v[152:153], v[152:153], v[152:153]
	v_pk_mul_f32 v[160:161], v[160:161], v[160:161]
	v_pk_mul_f32 v[156:157], v[166:167], v[166:167]
	v_pk_mul_f32 v[164:165], v[142:143], v[142:143]
	v_cvt_pk_fp8_f32 v140, v152, v153 op_sel:[0,0,1]
	v_cvt_pk_fp8_f32 v142, v160, v161
	v_cvt_pk_fp8_f32 v143, v156, v157
	v_cvt_pk_fp8_f32 v141, v168, v169 op_sel:[0,0,1]
	s_mov_b32 s23, s22
	v_cvt_pk_fp8_f32 v142, v172, v173 op_sel:[0,0,1]
	v_cvt_pk_fp8_f32 v143, v164, v165 op_sel:[0,0,1]
	v_or_b32_e32 v152, 32, v146
	v_mov_b64_e32 v[160:161], s[22:23]
	v_ashrrev_i32_e32 v153, 31, v152
	v_lshlrev_b64 v[152:153], 13, v[152:153]
	v_mfma_f32_16x16x32_fp8_fp8 v[156:159], v[140:141], v[160:161], 0
	v_lshl_add_u64 v[152:153], s[10:11], 0, v[152:153]
	v_lshl_add_u64 v[152:153], v[152:153], 0, v[144:145]
	global_store_dwordx4 v[152:153], v[140:143], off sc1
	s_nop 1
	v_mfma_f32_16x16x32_fp8_fp8 v[140:143], v[142:143], v[160:161], v[156:159]
	s_and_saveexec_b64 s[0:1], s[20:21]
	s_nop 6
	global_store_dwordx4 v[212:213], v[140:143], off offset:128 sc1
	s_or_b64 exec, exec, s[0:1]
	v_add_u32_e32 v156, 0xc0, v162
	s_nop 3
	ds_read2st64_b32 v[142:143], v156 offset1:4
	v_cvt_f32_i32_e32 v141, v81
	v_cvt_f32_i32_e32 v140, v80
	v_cvt_f32_i32_e32 v165, v75
	v_cvt_f32_i32_e32 v164, v74
	s_waitcnt lgkmcnt(0)
	v_mov_b32_e32 v158, v143
	v_pk_mul_f32 v[140:141], v[136:137], v[140:141]
	v_cvt_f32_i32_e32 v169, v71
	v_cvt_f32_i32_e32 v168, v70
	v_pk_fma_f32 v[140:141], v[140:141], v[142:143], v[158:159] op_sel_hi:[1,0,0]
	v_cvt_f32_i32_e32 v161, v73
	v_pk_mul_f32 v[166:167], v[140:141], v[140:141]
	v_pk_mul_f32 v[140:141], v[134:135], v[164:165]
	v_cvt_f32_i32_e32 v160, v72
	v_pk_fma_f32 v[140:141], v[140:141], v[142:143], v[158:159] op_sel_hi:[1,0,0]
	v_cvt_f32_i32_e32 v153, v83
	v_pk_mul_f32 v[170:171], v[140:141], v[140:141]
	v_pk_mul_f32 v[140:141], v[130:131], v[168:169]
	v_cvt_f32_i32_e32 v169, v65
	v_cvt_f32_i32_e32 v168, v64
	v_cvt_f32_i32_e32 v152, v82
	v_pk_mul_f32 v[160:161], v[132:133], v[160:161]
	v_cvt_f32_i32_e32 v165, v69
	v_cvt_f32_i32_e32 v164, v68
	v_pk_fma_f32 v[140:141], v[140:141], v[142:143], v[158:159] op_sel_hi:[1,0,0]
	v_pk_fma_f32 v[160:161], v[160:161], v[142:143], v[158:159] op_sel_hi:[1,0,0]
	v_cvt_f32_i32_e32 v173, v67
	v_cvt_f32_i32_e32 v172, v66
	v_pk_mul_f32 v[174:175], v[140:141], v[140:141]
	v_pk_mul_f32 v[140:141], v[124:125], v[168:169]
	v_pk_mul_f32 v[160:161], v[160:161], v[160:161]
	v_pk_fma_f32 v[168:169], v[140:141], v[142:143], v[158:159] op_sel_hi:[1,0,0]
	v_pk_mul_f32 v[152:153], v[138:139], v[152:153]
	v_cvt_pk_fp8_f32 v140, v166, v167
	v_cvt_pk_fp8_f32 v141, v160, v161
	v_pk_mul_f32 v[164:165], v[128:129], v[164:165]
	v_pk_fma_f32 v[152:153], v[152:153], v[142:143], v[158:159] op_sel_hi:[1,0,0]
	v_pk_fma_f32 v[164:165], v[164:165], v[142:143], v[158:159] op_sel_hi:[1,0,0]
	v_pk_mul_f32 v[172:173], v[126:127], v[172:173]
	v_pk_mul_f32 v[152:153], v[152:153], v[152:153]
	v_pk_mul_f32 v[164:165], v[164:165], v[164:165]
	v_pk_fma_f32 v[158:159], v[172:173], v[142:143], v[158:159] op_sel_hi:[1,0,0]
	v_pk_mul_f32 v[160:161], v[168:169], v[168:169]
	v_cvt_pk_fp8_f32 v140, v152, v153 op_sel:[0,0,1]
	v_cvt_pk_fp8_f32 v141, v170, v171 op_sel:[0,0,1]
	v_cvt_pk_fp8_f32 v142, v164, v165
	v_cvt_pk_fp8_f32 v143, v160, v161
	v_pk_mul_f32 v[152:153], v[158:159], v[158:159]
	v_or_b32_e32 v158, 48, v146
	v_cvt_pk_fp8_f32 v142, v174, v175 op_sel:[0,0,1]
	v_cvt_pk_fp8_f32 v143, v152, v153 op_sel:[0,0,1]
	v_ashrrev_i32_e32 v159, 31, v158
	v_mov_b64_e32 v[164:165], s[22:23]
	v_lshlrev_b64 v[152:153], 13, v[158:159]
	v_lshl_add_u64 v[152:153], s[10:11], 0, v[152:153]
	v_mfma_f32_16x16x32_fp8_fp8 v[158:161], v[140:141], v[164:165], 0
	v_lshl_add_u64 v[152:153], v[152:153], 0, v[144:145]
	global_store_dwordx4 v[152:153], v[140:143], off sc1
	s_nop 1
	v_mfma_f32_16x16x32_fp8_fp8 v[140:143], v[142:143], v[164:165], v[158:161]
	s_and_saveexec_b64 s[0:1], s[20:21]
	s_nop 6
	global_store_dwordx4 v[212:213], v[140:143], off offset:192 sc1
	s_or_b64 exec, exec, s[0:1]
	s_nop 4
	ds_read2st64_b32 v[140:141], v162 offset0:2 offset1:6
	v_cvt_f32_i32_e32 v143, v61
	v_cvt_f32_i32_e32 v153, v63
	v_cvt_f32_i32_e32 v152, v62
	v_cvt_f32_i32_e32 v142, v60
	v_cvt_f32_i32_e32 v161, v57
	v_cvt_f32_i32_e32 v165, v59
	v_cvt_f32_i32_e32 v164, v58
	v_cvt_f32_i32_e32 v160, v56
	v_cvt_f32_i32_e32 v167, v49
	v_cvt_f32_i32_e32 v169, v51
	v_cvt_f32_i32_e32 v168, v50
	v_cvt_f32_i32_e32 v166, v48
	v_cvt_f32_i32_e32 v171, v41
	v_cvt_f32_i32_e32 v173, v43
	v_cvt_f32_i32_e32 v172, v42
	v_cvt_f32_i32_e32 v170, v40
	v_pk_mul_f32 v[152:153], v[138:139], v[152:153]
	v_pk_mul_f32 v[142:143], v[136:137], v[142:143]
	s_waitcnt lgkmcnt(0)
	v_mov_b32_e32 v158, v141
	v_pk_mul_f32 v[164:165], v[134:135], v[164:165]
	v_pk_mul_f32 v[160:161], v[132:133], v[160:161]
	v_pk_mul_f32 v[168:169], v[130:131], v[168:169]
	v_pk_mul_f32 v[166:167], v[128:129], v[166:167]
	v_pk_mul_f32 v[172:173], v[126:127], v[172:173]
	v_pk_mul_f32 v[170:171], v[124:125], v[170:171]
	v_pk_fma_f32 v[142:143], v[142:143], v[140:141], v[158:159] op_sel_hi:[1,0,0]
	v_pk_fma_f32 v[152:153], v[152:153], v[140:141], v[158:159] op_sel_hi:[1,0,0]
	v_pk_fma_f32 v[160:161], v[160:161], v[140:141], v[158:159] op_sel_hi:[1,0,0]
	v_pk_fma_f32 v[164:165], v[164:165], v[140:141], v[158:159] op_sel_hi:[1,0,0]
	v_pk_fma_f32 v[166:167], v[166:167], v[140:141], v[158:159] op_sel_hi:[1,0,0]
	v_pk_fma_f32 v[168:169], v[168:169], v[140:141], v[158:159] op_sel_hi:[1,0,0]
	v_pk_fma_f32 v[170:171], v[170:171], v[140:141], v[158:159] op_sel_hi:[1,0,0]
	v_pk_fma_f32 v[140:141], v[172:173], v[140:141], v[158:159] op_sel_hi:[1,0,0]
	v_pk_mul_f32 v[142:143], v[142:143], v[142:143]
	v_pk_mul_f32 v[160:161], v[160:161], v[160:161]
	v_pk_mul_f32 v[158:159], v[170:171], v[170:171]
	v_pk_mul_f32 v[170:171], v[140:141], v[140:141]
	v_pk_mul_f32 v[152:153], v[152:153], v[152:153]
	v_cvt_pk_fp8_f32 v140, v142, v143
	v_cvt_pk_fp8_f32 v141, v160, v161
	v_pk_mul_f32 v[164:165], v[164:165], v[164:165]
	v_pk_mul_f32 v[166:167], v[166:167], v[166:167]
	v_cvt_pk_fp8_f32 v140, v152, v153 op_sel:[0,0,1]
	v_cvt_pk_fp8_f32 v142, v166, v167
	v_cvt_pk_fp8_f32 v143, v158, v159
	v_cvt_pk_fp8_f32 v141, v164, v165 op_sel:[0,0,1]
	v_pk_mul_f32 v[168:169], v[168:169], v[168:169]
	s_mov_b32 s23, s22
	v_cvt_pk_fp8_f32 v142, v168, v169 op_sel:[0,0,1]
	v_cvt_pk_fp8_f32 v143, v170, v171 op_sel:[0,0,1]
	v_lshlrev_b64 v[152:153], 13, v[146:147]
	v_mov_b64_e32 v[166:167], s[22:23]
	v_lshl_add_u64 v[152:153], s[10:11], 0, v[152:153]
	v_lshl_add_u64 v[152:153], v[152:153], 0, v[144:145]
	v_mfma_f32_16x16x32_fp8_fp8 v[158:161], v[140:141], v[166:167], 0
	v_add_co_u32_e32 v164, vcc, s56, v152
	s_nop 1
	v_addc_co_u32_e32 v165, vcc, 0, v153, vcc
	global_store_dwordx4 v[164:165], v[140:143], off sc1
	s_nop 1
	v_mfma_f32_16x16x32_fp8_fp8 v[140:143], v[142:143], v[166:167], v[158:161]
	s_and_saveexec_b64 s[0:1], s[20:21]
	s_nop 6
	global_store_dwordx4 v[212:213], v[140:143], off offset:512 sc1
	s_or_b64 exec, exec, s[0:1]
	ds_read2st64_b32 v[158:159], v154 offset0:2 offset1:6
	s_nop 3
	v_cvt_f32_i32_e32 v141, v53
	v_cvt_f32_i32_e32 v140, v52
	v_cvt_f32_i32_e32 v165, v47
	v_cvt_f32_i32_e32 v164, v46
	s_waitcnt lgkmcnt(0)
	v_mov_b32_e32 v154, v159
	v_pk_mul_f32 v[140:141], v[136:137], v[140:141]
	v_cvt_f32_i32_e32 v169, v35
	v_cvt_f32_i32_e32 v168, v34
	v_pk_fma_f32 v[140:141], v[140:141], v[158:159], v[154:155] op_sel_hi:[1,0,0]
	v_cvt_f32_i32_e32 v161, v45
	v_cvt_f32_i32_e32 v160, v44
	v_pk_mul_f32 v[166:167], v[140:141], v[140:141]
	v_pk_mul_f32 v[140:141], v[134:135], v[164:165]
	v_cvt_f32_i32_e32 v143, v55
	v_pk_fma_f32 v[140:141], v[140:141], v[158:159], v[154:155] op_sel_hi:[1,0,0]
	v_cvt_f32_i32_e32 v142, v54
	v_pk_mul_f32 v[170:171], v[140:141], v[140:141]
	v_pk_mul_f32 v[140:141], v[130:131], v[168:169]
	v_pk_mul_f32 v[160:161], v[132:133], v[160:161]
	v_cvt_f32_i32_e32 v165, v33
	v_cvt_f32_i32_e32 v164, v32
	v_pk_fma_f32 v[140:141], v[140:141], v[158:159], v[154:155] op_sel_hi:[1,0,0]
	v_cvt_f32_i32_e32 v169, v25
	v_cvt_f32_i32_e32 v168, v24
	v_pk_fma_f32 v[160:161], v[160:161], v[158:159], v[154:155] op_sel_hi:[1,0,0]
	v_pk_mul_f32 v[174:175], v[140:141], v[140:141]
	v_pk_mul_f32 v[160:161], v[160:161], v[160:161]
	v_cvt_pk_fp8_f32 v140, v166, v167
	v_pk_mul_f32 v[142:143], v[138:139], v[142:143]
	v_cvt_pk_fp8_f32 v141, v160, v161
	v_pk_fma_f32 v[142:143], v[142:143], v[158:159], v[154:155] op_sel_hi:[1,0,0]
	v_pk_mul_f32 v[164:165], v[128:129], v[164:165]
	v_cvt_f32_i32_e32 v173, v27
	v_cvt_f32_i32_e32 v172, v26
	v_pk_mul_f32 v[168:169], v[124:125], v[168:169]
	v_pk_mul_f32 v[142:143], v[142:143], v[142:143]
	v_pk_fma_f32 v[164:165], v[164:165], v[158:159], v[154:155] op_sel_hi:[1,0,0]
	v_pk_fma_f32 v[160:161], v[168:169], v[158:159], v[154:155] op_sel_hi:[1,0,0]
	v_pk_mul_f32 v[164:165], v[164:165], v[164:165]
	v_pk_mul_f32 v[160:161], v[160:161], v[160:161]
	v_cvt_pk_fp8_f32 v140, v142, v143 op_sel:[0,0,1]
	v_cvt_pk_fp8_f32 v141, v170, v171 op_sel:[0,0,1]
	v_cvt_pk_fp8_f32 v142, v164, v165
	v_cvt_pk_fp8_f32 v143, v160, v161
	v_pk_mul_f32 v[172:173], v[126:127], v[172:173]
	v_mov_b64_e32 v[164:165], s[22:23]
	v_pk_fma_f32 v[158:159], v[172:173], v[158:159], v[154:155] op_sel_hi:[1,0,0]
	v_cvt_pk_fp8_f32 v142, v174, v175 op_sel:[0,0,1]
	v_pk_mul_f32 v[158:159], v[158:159], v[158:159]
	v_add_co_u32_e32 v152, vcc, 0x120000, v152
	v_cvt_pk_fp8_f32 v143, v158, v159 op_sel:[0,0,1]
	v_mfma_f32_16x16x32_fp8_fp8 v[158:161], v[140:141], v[164:165], 0
	v_addc_co_u32_e32 v153, vcc, 0, v153, vcc
	global_store_dwordx4 v[152:153], v[140:143], off sc1
	s_nop 1
	v_mfma_f32_16x16x32_fp8_fp8 v[140:143], v[142:143], v[164:165], v[158:161]
	s_and_saveexec_b64 s[0:1], s[20:21]
	s_nop 6
	global_store_dwordx4 v[212:213], v[140:143], off offset:576 sc1
	s_or_b64 exec, exec, s[0:1]
	s_nop 4
	ds_read2st64_b32 v[140:141], v155 offset0:2 offset1:6
	v_cvt_f32_i32_e32 v143, v37
	v_cvt_f32_i32_e32 v153, v39
	v_cvt_f32_i32_e32 v152, v38
	v_cvt_f32_i32_e32 v142, v36
	v_cvt_f32_i32_e32 v159, v29
	v_cvt_f32_i32_e32 v161, v31
	v_cvt_f32_i32_e32 v160, v30
	v_cvt_f32_i32_e32 v158, v28
	v_cvt_f32_i32_e32 v165, v17
	v_cvt_f32_i32_e32 v167, v19
	v_cvt_f32_i32_e32 v166, v18
	v_cvt_f32_i32_e32 v164, v16
	v_cvt_f32_i32_e32 v169, v9
	v_cvt_f32_i32_e32 v171, v11
	v_cvt_f32_i32_e32 v170, v10
	v_cvt_f32_i32_e32 v168, v8
	v_pk_mul_f32 v[152:153], v[138:139], v[152:153]
	v_pk_mul_f32 v[142:143], v[136:137], v[142:143]
	s_waitcnt lgkmcnt(0)
	v_mov_b32_e32 v154, v141
	v_pk_mul_f32 v[160:161], v[134:135], v[160:161]
	v_pk_mul_f32 v[158:159], v[132:133], v[158:159]
	v_pk_mul_f32 v[166:167], v[130:131], v[166:167]
	v_pk_mul_f32 v[164:165], v[128:129], v[164:165]
	v_pk_mul_f32 v[170:171], v[126:127], v[170:171]
	v_pk_mul_f32 v[168:169], v[124:125], v[168:169]
	v_pk_fma_f32 v[142:143], v[142:143], v[140:141], v[154:155] op_sel_hi:[1,0,0]
	v_pk_fma_f32 v[152:153], v[152:153], v[140:141], v[154:155] op_sel_hi:[1,0,0]
	v_pk_fma_f32 v[158:159], v[158:159], v[140:141], v[154:155] op_sel_hi:[1,0,0]
	v_pk_fma_f32 v[160:161], v[160:161], v[140:141], v[154:155] op_sel_hi:[1,0,0]
	v_pk_fma_f32 v[164:165], v[164:165], v[140:141], v[154:155] op_sel_hi:[1,0,0]
	v_pk_fma_f32 v[166:167], v[166:167], v[140:141], v[154:155] op_sel_hi:[1,0,0]
	v_pk_fma_f32 v[168:169], v[168:169], v[140:141], v[154:155] op_sel_hi:[1,0,0]
	v_pk_fma_f32 v[140:141], v[170:171], v[140:141], v[154:155] op_sel_hi:[1,0,0]
	v_pk_mul_f32 v[142:143], v[142:143], v[142:143]
	v_pk_mul_f32 v[158:159], v[158:159], v[158:159]
	v_pk_mul_f32 v[154:155], v[168:169], v[168:169]
	v_pk_mul_f32 v[168:169], v[140:141], v[140:141]
	v_pk_mul_f32 v[152:153], v[152:153], v[152:153]
	v_cvt_pk_fp8_f32 v140, v142, v143
	v_cvt_pk_fp8_f32 v141, v158, v159
	v_pk_mul_f32 v[160:161], v[160:161], v[160:161]
	v_pk_mul_f32 v[164:165], v[164:165], v[164:165]
	v_cvt_pk_fp8_f32 v140, v152, v153 op_sel:[0,0,1]
	v_cvt_pk_fp8_f32 v142, v164, v165
	v_cvt_pk_fp8_f32 v143, v154, v155
	v_cvt_pk_fp8_f32 v141, v160, v161 op_sel:[0,0,1]
	v_pk_mul_f32 v[166:167], v[166:167], v[166:167]
	v_lshlrev_b64 v[152:153], 13, v[146:147]
	v_cvt_pk_fp8_f32 v142, v166, v167 op_sel:[0,0,1]
	v_cvt_pk_fp8_f32 v143, v168, v169 op_sel:[0,0,1]
	s_mov_b32 s23, s22
	v_lshl_add_u64 v[152:153], s[10:11], 0, v[152:153]
	v_mov_b64_e32 v[160:161], s[22:23]
	v_lshl_add_u64 v[158:159], v[152:153], 0, v[144:145]
	v_add_co_u32_e32 v158, vcc, s57, v158
	v_mfma_f32_16x16x32_fp8_fp8 v[152:155], v[140:141], v[160:161], 0
	s_nop 0
	v_addc_co_u32_e32 v159, vcc, 0, v159, vcc
	global_store_dwordx4 v[158:159], v[140:143], off sc1
	s_nop 1
	v_mfma_f32_16x16x32_fp8_fp8 v[140:143], v[142:143], v[160:161], v[152:155]
	s_and_saveexec_b64 s[0:1], s[20:21]
	s_nop 6
	global_store_dwordx4 v[212:213], v[140:143], off offset:640 sc1
	s_or_b64 exec, exec, s[0:1]
	v_cvt_f32_i32_e32 v153, v23
	v_cvt_f32_i32_e32 v152, v22
	v_cvt_f32_i32_e32 v155, v15
	v_cvt_f32_i32_e32 v154, v14
	s_nop 0
	ds_read2st64_b32 v[140:141], v156 offset0:2 offset1:6
	v_pk_mul_f32 v[138:139], v[138:139], v[152:153]
	v_cvt_f32_i32_e32 v153, v13
	v_cvt_f32_i32_e32 v152, v12
	v_cvt_f32_i32_e32 v143, v21
	v_cvt_f32_i32_e32 v142, v20
	v_pk_mul_f32 v[134:135], v[134:135], v[154:155]
	v_pk_mul_f32 v[132:133], v[132:133], v[152:153]
	v_cvt_f32_i32_e32 v153, v5
	v_cvt_f32_i32_e32 v152, v4
	v_cvt_f32_i32_e32 v155, v7
	v_cvt_f32_i32_e32 v154, v6
	v_pk_mul_f32 v[136:137], v[136:137], v[142:143]
	v_pk_mul_f32 v[128:129], v[128:129], v[152:153]
	v_cvt_f32_i32_e32 v153, v1
	v_cvt_f32_i32_e32 v152, v0
	s_waitcnt lgkmcnt(0)
	v_mov_b32_e32 v142, v141
	v_pk_fma_f32 v[136:137], v[136:137], v[140:141], v[142:143] op_sel_hi:[1,0,0]
	v_pk_fma_f32 v[132:133], v[132:133], v[140:141], v[142:143] op_sel_hi:[1,0,0]
	v_pk_mul_f32 v[130:131], v[130:131], v[154:155]
	v_cvt_f32_i32_e32 v155, v3
	v_cvt_f32_i32_e32 v154, v2
	v_pk_mul_f32 v[124:125], v[124:125], v[152:153]
	v_pk_mul_f32 v[136:137], v[136:137], v[136:137]
	v_pk_mul_f32 v[132:133], v[132:133], v[132:133]
	v_pk_fma_f32 v[152:153], v[124:125], v[140:141], v[142:143] op_sel_hi:[1,0,0]
	v_pk_fma_f32 v[138:139], v[138:139], v[140:141], v[142:143] op_sel_hi:[1,0,0]
	v_cvt_pk_fp8_f32 v124, v136, v137
	v_cvt_pk_fp8_f32 v125, v132, v133
	v_pk_fma_f32 v[134:135], v[134:135], v[140:141], v[142:143] op_sel_hi:[1,0,0]
	v_pk_fma_f32 v[128:129], v[128:129], v[140:141], v[142:143] op_sel_hi:[1,0,0]
	v_pk_mul_f32 v[126:127], v[126:127], v[154:155]
	v_pk_mul_f32 v[138:139], v[138:139], v[138:139]
	v_pk_mul_f32 v[134:135], v[134:135], v[134:135]
	v_pk_mul_f32 v[128:129], v[128:129], v[128:129]
	v_pk_fma_f32 v[132:133], v[126:127], v[140:141], v[142:143] op_sel_hi:[1,0,0]
	v_pk_mul_f32 v[136:137], v[152:153], v[152:153]
	v_cvt_pk_fp8_f32 v124, v138, v139 op_sel:[0,0,1]
	v_cvt_pk_fp8_f32 v125, v134, v135 op_sel:[0,0,1]
	v_cvt_pk_fp8_f32 v126, v128, v129
	v_cvt_pk_fp8_f32 v127, v136, v137
	v_pk_fma_f32 v[130:131], v[130:131], v[140:141], v[142:143] op_sel_hi:[1,0,0]
	v_pk_mul_f32 v[128:129], v[132:133], v[132:133]
	v_pk_mul_f32 v[130:131], v[130:131], v[130:131]
	v_cvt_pk_fp8_f32 v127, v128, v129 op_sel:[0,0,1]
	v_cvt_pk_fp8_f32 v126, v130, v131 op_sel:[0,0,1]
	v_mov_b64_e32 v[134:135], s[22:23]
	v_add_u32_e32 v160, 0xb0, v146
	v_ashrrev_i32_e32 v161, 31, v160
	v_mfma_f32_16x16x32_fp8_fp8 v[128:131], v[124:125], v[134:135], 0
	v_lshlrev_b64 v[132:133], 13, v[160:161]
	v_lshl_add_u64 v[132:133], s[10:11], 0, v[132:133]
	v_lshl_add_u64 v[132:133], v[132:133], 0, v[144:145]
	v_mfma_f32_16x16x32_fp8_fp8 v[140:143], v[126:127], v[134:135], v[128:131]
	s_mov_b64 s[0:1], s[20:21]
	global_store_dwordx4 v[132:133], v[124:127], off sc1

	.amdhsa_kernel _ZN2rb6k_gemmILi2ENS_7SchedP1ENS_5EpiP1EEEvT0_T1_
		.amdhsa_group_segment_fixed_size 0
		.amdhsa_private_segment_fixed_size 0
		.amdhsa_kernarg_size 88
		.amdhsa_user_sgpr_count 2
		.amdhsa_user_sgpr_dispatch_ptr 0
		.amdhsa_user_sgpr_queue_ptr 0
		.amdhsa_user_sgpr_kernarg_segment_ptr 1
		.amdhsa_user_sgpr_dispatch_id 0
		.amdhsa_user_sgpr_kernarg_preload_length 0
		.amdhsa_user_sgpr_kernarg_preload_offset 0
		.amdhsa_user_sgpr_private_segment_size 0
		.amdhsa_uses_dynamic_stack 0
		.amdhsa_enable_private_segment 0
		.amdhsa_system_sgpr_workgroup_id_x 1
		.amdhsa_system_sgpr_workgroup_id_y 0
		.amdhsa_system_sgpr_workgroup_id_z 0
		.amdhsa_system_sgpr_workgroup_info 0
		.amdhsa_system_vgpr_workitem_id 0
		.amdhsa_next_free_vgpr 214
		.amdhsa_next_free_sgpr 80
		.amdhsa_accum_offset 216
		.amdhsa_reserve_vcc 1
		.amdhsa_float_round_mode_32 0
		.amdhsa_float_round_mode_16_64 0
		.amdhsa_float_denorm_mode_32 3
		.amdhsa_float_denorm_mode_16_64 3
		.amdhsa_dx10_clamp 1
		.amdhsa_ieee_mode 1
		.amdhsa_fp16_overflow 0
		.amdhsa_tg_split 0
		.amdhsa_exception_fp_ieee_invalid_op 0
		.amdhsa_exception_fp_denorm_src 0
		.amdhsa_exception_fp_ieee_div_zero 0
		.amdhsa_exception_fp_ieee_overflow 0
		.amdhsa_exception_fp_ieee_underflow 0
		.amdhsa_exception_fp_ieee_inexact 0
		.amdhsa_exception_int_div_zero 0
	.end_amdhsa_kernel

amdhsa.kernels:
  - .agpr_count:     0
    .args:
      - .actual_access:  read_only
        .address_space:  global
        .offset:         0
        .size:           8
        .value_kind:     global_buffer
      - .actual_access:  read_only
        .address_space:  global
        .offset:         8
        .size:           8
        .value_kind:     global_buffer
      - .actual_access:  read_only
        .address_space:  global
        .offset:         16
        .size:           8
        .value_kind:     global_buffer
      - .actual_access:  read_only
        .address_space:  global
        .offset:         24
        .size:           8
        .value_kind:     global_buffer
      - .actual_access:  read_only
        .address_space:  global
        .offset:         32
        .size:           8
        .value_kind:     global_buffer
      - .actual_access:  read_only
        .address_space:  global
        .offset:         40
        .size:           8
        .value_kind:     global_buffer
      - .actual_access:  read_only
        .address_space:  global
        .offset:         48
        .size:           8
        .value_kind:     global_buffer
      - .actual_access:  read_only
        .address_space:  global
        .offset:         56
        .size:           8
        .value_kind:     global_buffer
      - .actual_access:  write_only
        .address_space:  global
        .offset:         64
        .size:           8
        .value_kind:     global_buffer
      - .offset:         72
        .size:           4
        .value_kind:     by_value
    .group_segment_fixed_size: 32768
    .kernarg_segment_align: 8
    .kernarg_segment_size: 76
    .language:       OpenCL C
    .language_version:
      - 2
      - 0
    .max_flat_workgroup_size: 256
    .name:           _ZN2rb6k_prepEPKfS1_S1_S1_S1_S1_S1_S1_Phi
    .private_segment_fixed_size: 0
    .sgpr_count:     22
    .sgpr_spill_count: 0
    .symbol:         _ZN2rb6k_prepEPKfS1_S1_S1_S1_S1_S1_S1_Phi.kd
    .uniform_work_group_size: 1
    .uses_dynamic_stack: false
    .vgpr_count:     100
    .vgpr_spill_count: 0
    .wavefront_size: 64
  - .agpr_count:     0
    .args:
      - .address_space:  global
        .offset:         0
        .size:           8
        .value_kind:     global_buffer
      - .actual_access:  read_only
        .address_space:  global
        .offset:         8
        .size:           8
        .value_kind:     global_buffer
    .group_segment_fixed_size: 0
    .kernarg_segment_align: 8
    .kernarg_segment_size: 16
    .language:       OpenCL C
    .language_version:
      - 2
      - 0
    .max_flat_workgroup_size: 256
    .name:           _ZN2rb5k_midEPhPKf
    .private_segment_fixed_size: 0
    .sgpr_count:     20
    .sgpr_spill_count: 0
    .symbol:         _ZN2rb5k_midEPhPKf.kd
    .uniform_work_group_size: 1
    .uses_dynamic_stack: false
    .vgpr_count:     86
    .vgpr_spill_count: 0
    .wavefront_size: 64
  - .agpr_count:     0
    .args:
      - .offset:         0
        .size:           24
        .value_kind:     by_value
      - .offset:         24
        .size:           64
        .value_kind:     by_value
    .group_segment_fixed_size: 0
    .kernarg_segment_align: 8
    .kernarg_segment_size: 88
    .language:       OpenCL C
    .language_version:
      - 2
      - 0
    .max_flat_workgroup_size: 512
    .name:           _ZN2rb6k_gemmILi2ENS_7SchedP1ENS_5EpiP1EEEvT0_T1_
    .private_segment_fixed_size: 0
    .sgpr_count:     86
    .sgpr_spill_count: 0
    .symbol:         _ZN2rb6k_gemmILi2ENS_7SchedP1ENS_5EpiP1EEEvT0_T1_.kd
    .uniform_work_group_size: 1
    .uses_dynamic_stack: false
    .vgpr_count:     214
    .vgpr_spill_count: 0
    .wavefront_size: 64
  - .agpr_count:     0
    .args:
      - .offset:         0
        .size:           24
        .value_kind:     by_value
      - .offset:         24
        .size:           16
        .value_kind:     by_value
    .group_segment_fixed_size: 0
    .kernarg_segment_align: 8
    .kernarg_segment_size: 40
    .language:       OpenCL C
    .language_version:
      - 2
      - 0
    .max_flat_workgroup_size: 512
    .name:           _ZN2rb6k_gemmILi1ENS_7SchedP2ENS_7EpiSlabEEEvT0_T1_
    .private_segment_fixed_size: 0
    .sgpr_count:     73
    .sgpr_spill_count: 0
    .symbol:         _ZN2rb6k_gemmILi1ENS_7SchedP2ENS_7EpiSlabEEEvT0_T1_.kd
    .uniform_work_group_size: 1
    .uses_dynamic_stack: false
    .vgpr_count:     210
    .vgpr_spill_count: 0
    .wavefront_size: 64
  - .agpr_count:     0
    .args:
      - .offset:         0
        .size:           32
        .value_kind:     by_value
      - .offset:         32
        .size:           16
        .value_kind:     by_value
    .group_segment_fixed_size: 0
    .kernarg_segment_align: 8
    .kernarg_segment_size: 48
    .language:       OpenCL C
    .language_version:
      - 2
      - 0
    .max_flat_workgroup_size: 512
    .name:           _ZN2rb6k_gemmILi1ENS_6SchedGILb1EEENS_5EpiP3EEEvT0_T1_
    .private_segment_fixed_size: 0
    .sgpr_count:     62
    .sgpr_spill_count: 0
    .symbol:         _ZN2rb6k_gemmILi1ENS_6SchedGILb1EEENS_5EpiP3EEEvT0_T1_.kd
    .uniform_work_group_size: 1
    .uses_dynamic_stack: false
    .vgpr_count:     207
    .vgpr_spill_count: 0
    .wavefront_size: 64
  - .agpr_count:     0
    .args:
      - .offset:         0
        .size:           32
        .value_kind:     by_value
      - .offset:         32
        .size:           48
        .value_kind:     by_value
    .group_segment_fixed_size: 0
    .kernarg_segment_align: 8
    .kernarg_segment_size: 80
    .language:       OpenCL C
    .language_version:
      - 2
      - 0
    .max_flat_workgroup_size: 512
    .name:           _ZN2rb6k_gemmILi1ENS_6SchedGILb1EEENS_6EpiOutEEEvT0_T1_
    .private_segment_fixed_size: 0
    .sgpr_count:     62
    .sgpr_spill_count: 0
    .symbol:         _ZN2rb6k_gemmILi1ENS_6SchedGILb1EEENS_6EpiOutEEEvT0_T1_.kd
    .uniform_work_group_size: 1
    .uses_dynamic_stack: false
    .vgpr_count:     205
    .vgpr_spill_count: 0
    .wavefront_size: 64
  - .agpr_count:     0
    .args:
      - .offset:         0
        .size:           24
        .value_kind:     by_value
      - .offset:         24
        .size:           1
        .value_kind:     by_value
    .group_segment_fixed_size: 0
    .kernarg_segment_align: 8
    .kernarg_segment_size: 28
    .language:       OpenCL C
    .language_version:
      - 2
      - 0
    .max_flat_workgroup_size: 512
    .name:           _ZN2rb6k_gemmILi2ENS_7SchedP1ENS_7EpiNullEEEvT0_T1_
    .private_segment_fixed_size: 0
    .sgpr_count:     66
    .sgpr_spill_count: 0
    .symbol:         _ZN2rb6k_gemmILi2ENS_7SchedP1ENS_7EpiNullEEEvT0_T1_.kd
    .uniform_work_group_size: 1
    .uses_dynamic_stack: false
    .vgpr_count:     205
    .vgpr_spill_count: 0
    .wavefront_size: 64
